# baseline (speedup 1.0000x reference)
_Z9fc_kernelPKDv8_DF16_S1_Pf:
	s_cmp_gt_u32 s2, 511
	s_cbranch_scc1 .Lfc_exit
	s_load_dwordx4 s[4:7], s[0:1], 0x0
	s_load_dwordx2 s[16:17], s[0:1], 0x10
	v_and_b32_e32 v1, 63, v0
	v_lshrrev_b32_e32 v113, 6, v0
	v_and_b32_e32 v89, 31, v0
	v_bfe_u32 v90, v0, 5, 1
	v_lshlrev_b32_e32 v116, 4, v0
	v_lshlrev_b32_e32 v112, 4, v1
	v_lshlrev_b32_e32 v4, 12, v90
	v_lshl_or_b32 v4, v113, 8, v4
	v_lshl_or_b32 v4, v89, 2, v4
	v_add_u32_e32 v102, 0xe000, v4
	v_lshlrev_b32_e32 v5, 12, v113
	s_mov_b32 s3, 0xe000
	v_add3_u32 v103, v5, v112, s3
	v_mul_u32_u24_e32 v6, 0xc3500, v113
	v_add_u32_e32 v104, v6, v112
	v_add_u32_e32 v105, 0x30d40, v104
	v_add_u32_e32 v106, 0x61a80, v104
	v_add_u32_e32 v107, 0x927c0, v104
	v_add_u32_e32 v108, 0x30d400, v104
	v_add_u32_e32 v109, 0x30d400, v105
	v_add_u32_e32 v110, 0x30d400, v106
	v_add_u32_e32 v111, 0x30d400, v107
	v_mul_u32_u24_e32 v7, 0x3800, v113
	v_add_u32_e32 v114, v7, v112
	v_cmp_gt_u32_e64 s[34:35], 20, v1
	s_mov_b32 s20, 0
	s_mov_b32 s22, -1
	s_waitcnt lgkmcnt(0)
.Lfc_seg:
	s_lshl_b32 s29, s20, 9
	s_and_b32 s3, s2, 7
	s_lshl_b32 s3, s3, 6
	s_add_i32 s29, s29, s3
	s_lshr_b32 s3, s2, 3
	s_add_i32 s29, s29, s3
	s_mov_b32 s26, 0
	s_mov_b32 s23, 8
	s_cmp_lt_u32 s20, 6
	s_cbranch_scc1 .Lfc_full
	s_lshr_b32 s29, s2, 3
	s_add_i32 s29, s29, 0xc00
	s_and_b32 s26, s2, 7
	s_mov_b32 s23, 1
.Lfc_full:
	s_mul_hi_u32 s27, s29, 0x5397829d
	s_lshr_b32 s27, s27, 6
	s_mul_i32 s3, s27, 0xc4
	s_sub_i32 s28, s29, s3
	s_mul_i32 s3, s28, 0xe000
	v_add_u32_e32 v117, s3, v114
	v_add_u32_e32 v118, 0x1000, v117
	v_add_u32_e32 v119, 0x2000, v117
	v_add_u32_e32 v115, 0x3000, v117
	global_load_dwordx4 v[32:35], v117, s[4:5]
	global_load_dwordx4 v[36:39], v117, s[4:5] offset:1024
	global_load_dwordx4 v[40:43], v117, s[4:5] offset:2048
	global_load_dwordx4 v[44:47], v117, s[4:5] offset:3072
	global_load_dwordx4 v[48:51], v118, s[4:5]
	global_load_dwordx4 v[52:55], v118, s[4:5] offset:1024
	global_load_dwordx4 v[56:59], v118, s[4:5] offset:2048
	global_load_dwordx4 v[60:63], v118, s[4:5] offset:3072
	global_load_dwordx4 v[64:67], v119, s[4:5]
	global_load_dwordx4 v[68:71], v119, s[4:5] offset:1024
	global_load_dwordx4 v[72:75], v119, s[4:5] offset:2048
	global_load_dwordx4 v[76:79], v119, s[4:5] offset:3072
	global_load_dwordx4 v[80:83], v115, s[4:5]
	global_load_dwordx4 v[84:87], v115, s[4:5] offset:1024
	s_cmp_eq_u32 s27, s22
	s_cbranch_scc1 .Lfc_noA
	s_mov_b32 s22, s27
	s_mul_i32 s3, s27, 0xe000
	s_add_u32 s30, s6, s3
	s_addc_u32 s31, s7, 0
	global_load_dwordx4 v[152:155], v116, s[30:31]
	s_add_u32 s30, s30, 0x1000
	s_addc_u32 s31, s31, 0
	global_load_dwordx4 v[156:159], v116, s[30:31]
	s_add_u32 s30, s30, 0x1000
	s_addc_u32 s31, s31, 0
	global_load_dwordx4 v[160:163], v116, s[30:31]
	s_add_u32 s30, s30, 0x1000
	s_addc_u32 s31, s31, 0
	global_load_dwordx4 v[164:167], v116, s[30:31]
	s_add_u32 s30, s30, 0x1000
	s_addc_u32 s31, s31, 0
	global_load_dwordx4 v[168:171], v116, s[30:31]
	s_add_u32 s30, s30, 0x1000
	s_addc_u32 s31, s31, 0
	global_load_dwordx4 v[172:175], v116, s[30:31]
	s_add_u32 s30, s30, 0x1000
	s_addc_u32 s31, s31, 0
	global_load_dwordx4 v[176:179], v116, s[30:31]
	s_add_u32 s30, s30, 0x1000
	s_addc_u32 s31, s31, 0
	global_load_dwordx4 v[180:183], v116, s[30:31]
	s_add_u32 s30, s30, 0x1000
	s_addc_u32 s31, s31, 0
	global_load_dwordx4 v[184:187], v116, s[30:31]
	s_add_u32 s30, s30, 0x1000
	s_addc_u32 s31, s31, 0
	global_load_dwordx4 v[188:191], v116, s[30:31]
	s_add_u32 s30, s30, 0x1000
	s_addc_u32 s31, s31, 0
	global_load_dwordx4 v[192:195], v116, s[30:31]
	s_add_u32 s30, s30, 0x1000
	s_addc_u32 s31, s31, 0
	global_load_dwordx4 v[196:199], v116, s[30:31]
	s_add_u32 s30, s30, 0x1000
	s_addc_u32 s31, s31, 0
	global_load_dwordx4 v[200:203], v116, s[30:31]
	s_add_u32 s30, s30, 0x1000
	s_addc_u32 s31, s31, 0
	global_load_dwordx4 v[204:207], v116, s[30:31]
	s_barrier
	s_waitcnt vmcnt(0)
	ds_write_b128 v116, v[152:155]
	ds_write_b128 v116, v[156:159] offset:4096
	ds_write_b128 v116, v[160:163] offset:8192
	ds_write_b128 v116, v[164:167] offset:12288
	ds_write_b128 v116, v[168:171] offset:16384
	ds_write_b128 v116, v[172:175] offset:20480
	ds_write_b128 v116, v[176:179] offset:24576
	ds_write_b128 v116, v[180:183] offset:28672
	ds_write_b128 v116, v[184:187] offset:32768
	ds_write_b128 v116, v[188:191] offset:36864
	ds_write_b128 v116, v[192:195] offset:40960
	ds_write_b128 v116, v[196:199] offset:45056
	ds_write_b128 v116, v[200:203] offset:49152
	ds_write_b128 v116, v[204:207] offset:53248
.Lfc_noA:
	s_lshl_b32 s3, s27, 8
	s_lshl_b32 s30, s26, 5
	s_add_i32 s3, s3, s30
	s_mul_i32 s3, s3, 0x30d40
	s_lshl_b32 s30, s28, 10
	s_add_u32 s3, s3, s30
	s_add_u32 s8, s16, s3
	s_addc_u32 s9, s17, 0
	s_mul_i32 s3, s26, 0x1c00
	v_add_u32_e32 v88, s3, v112
	s_mov_b64 s[24:25], -1
	s_cmp_eq_u32 s28, 195
	s_cselect_b64 s[24:25], s[34:35], s[24:25]
	s_mov_b32 s0, 0
	s_waitcnt vmcnt(0) lgkmcnt(0)
	s_barrier
.Lfc_step:
	ds_read_b128 v[120:123], v88
	ds_read_b128 v[124:127], v88 offset:1024
	ds_read_b128 v[128:131], v88 offset:2048
	ds_read_b128 v[132:135], v88 offset:3072
	ds_read_b128 v[136:139], v88 offset:4096
	ds_read_b128 v[140:143], v88 offset:5120
	ds_read_b128 v[144:147], v88 offset:6144
	v_add_u32_e32 v88, 0x1c00, v88
	s_waitcnt lgkmcnt(6)
	v_mfma_f32_32x32x16_f16 v[0:15], v[120:123], v[32:35], 0
	v_mfma_f32_32x32x16_f16 v[16:31], v[120:123], v[60:63], 0
	s_waitcnt lgkmcnt(5)
	v_mfma_f32_32x32x16_f16 v[0:15], v[124:127], v[36:39], v[0:15]
	v_mfma_f32_32x32x16_f16 v[16:31], v[124:127], v[64:67], v[16:31]
	s_waitcnt lgkmcnt(4)
	v_mfma_f32_32x32x16_f16 v[0:15], v[128:131], v[40:43], v[0:15]
	v_mfma_f32_32x32x16_f16 v[16:31], v[128:131], v[68:71], v[16:31]
	s_waitcnt lgkmcnt(3)
	v_mfma_f32_32x32x16_f16 v[0:15], v[132:135], v[44:47], v[0:15]
	v_mfma_f32_32x32x16_f16 v[16:31], v[132:135], v[72:75], v[16:31]
	s_waitcnt lgkmcnt(2)
	v_mfma_f32_32x32x16_f16 v[0:15], v[136:139], v[48:51], v[0:15]
	v_mfma_f32_32x32x16_f16 v[16:31], v[136:139], v[76:79], v[16:31]
	s_waitcnt lgkmcnt(1)
	v_mfma_f32_32x32x16_f16 v[0:15], v[140:143], v[52:55], v[0:15]
	v_mfma_f32_32x32x16_f16 v[16:31], v[140:143], v[80:83], v[16:31]
	s_waitcnt lgkmcnt(0)
	v_mfma_f32_32x32x16_f16 v[0:15], v[144:147], v[56:59], v[0:15]
	v_mfma_f32_32x32x16_f16 v[16:31], v[144:147], v[84:87], v[16:31]
	s_nop 11
	s_barrier
	ds_write_b32 v102, v0 offset:0
	ds_write_b32 v102, v1 offset:1024
	ds_write_b32 v102, v2 offset:2048
	ds_write_b32 v102, v3 offset:3072
	ds_write_b32 v102, v4 offset:8192
	ds_write_b32 v102, v5 offset:9216
	ds_write_b32 v102, v6 offset:10240
	ds_write_b32 v102, v7 offset:11264
	ds_write_b32 v102, v16 offset:128
	ds_write_b32 v102, v17 offset:1152
	ds_write_b32 v102, v18 offset:2176
	ds_write_b32 v102, v19 offset:3200
	ds_write_b32 v102, v20 offset:8320
	ds_write_b32 v102, v21 offset:9344
	ds_write_b32 v102, v22 offset:10368
	ds_write_b32 v102, v23 offset:11392
	s_waitcnt lgkmcnt(0)
	s_barrier
	ds_read_b128 v[0:3], v103
	ds_read_b128 v[4:7], v103 offset:1024
	ds_read_b128 v[16:19], v103 offset:2048
	ds_read_b128 v[20:23], v103 offset:3072
	s_mov_b64 exec, s[24:25]
	s_waitcnt lgkmcnt(3)
	global_store_dwordx4 v104, v[0:3], s[8:9]
	s_waitcnt lgkmcnt(2)
	global_store_dwordx4 v105, v[4:7], s[8:9]
	s_waitcnt lgkmcnt(1)
	global_store_dwordx4 v106, v[16:19], s[8:9]
	s_waitcnt lgkmcnt(0)
	global_store_dwordx4 v107, v[20:23], s[8:9]
	s_mov_b64 exec, -1
	s_barrier
	ds_write_b32 v102, v8 offset:0
	ds_write_b32 v102, v9 offset:1024
	ds_write_b32 v102, v10 offset:2048
	ds_write_b32 v102, v11 offset:3072
	ds_write_b32 v102, v12 offset:8192
	ds_write_b32 v102, v13 offset:9216
	ds_write_b32 v102, v14 offset:10240
	ds_write_b32 v102, v15 offset:11264
	ds_write_b32 v102, v24 offset:128
	ds_write_b32 v102, v25 offset:1152
	ds_write_b32 v102, v26 offset:2176
	ds_write_b32 v102, v27 offset:3200
	ds_write_b32 v102, v28 offset:8320
	ds_write_b32 v102, v29 offset:9344
	ds_write_b32 v102, v30 offset:10368
	ds_write_b32 v102, v31 offset:11392
	s_waitcnt lgkmcnt(0)
	s_barrier
	ds_read_b128 v[8:11], v103
	ds_read_b128 v[12:15], v103 offset:1024
	ds_read_b128 v[24:27], v103 offset:2048
	ds_read_b128 v[28:31], v103 offset:3072
	s_mov_b64 exec, s[24:25]
	s_waitcnt lgkmcnt(3)
	global_store_dwordx4 v108, v[8:11], s[8:9]
	s_waitcnt lgkmcnt(2)
	global_store_dwordx4 v109, v[12:15], s[8:9]
	s_waitcnt lgkmcnt(1)
	global_store_dwordx4 v110, v[24:27], s[8:9]
	s_waitcnt lgkmcnt(0)
	global_store_dwordx4 v111, v[28:31], s[8:9]
	s_mov_b64 exec, -1
	s_add_u32 s8, s8, 0x61a800
	s_addc_u32 s9, s9, 0
	s_add_i32 s0, s0, 1
	s_cmp_lt_u32 s0, s23
	s_cbranch_scc1 .Lfc_step
	s_add_i32 s20, s20, 1
	s_cmp_lt_u32 s20, 7
	s_cbranch_scc1 .Lfc_seg

	.amdhsa_kernel _Z9fc_kernelPKDv8_DF16_S1_Pf
		.amdhsa_group_segment_fixed_size 73728
		.amdhsa_private_segment_fixed_size 0
		.amdhsa_kernarg_size 24
		.amdhsa_user_sgpr_count 2
		.amdhsa_user_sgpr_dispatch_ptr 0
		.amdhsa_user_sgpr_queue_ptr 0
		.amdhsa_user_sgpr_kernarg_segment_ptr 1
		.amdhsa_user_sgpr_dispatch_id 0
		.amdhsa_user_sgpr_kernarg_preload_length 0
		.amdhsa_user_sgpr_kernarg_preload_offset 0
		.amdhsa_user_sgpr_private_segment_size 0
		.amdhsa_uses_dynamic_stack 0
		.amdhsa_enable_private_segment 0
		.amdhsa_system_sgpr_workgroup_id_x 1
		.amdhsa_system_sgpr_workgroup_id_y 0
		.amdhsa_system_sgpr_workgroup_id_z 0
		.amdhsa_system_sgpr_workgroup_info 0
		.amdhsa_system_vgpr_workitem_id 0
		.amdhsa_next_free_vgpr 208
		.amdhsa_next_free_sgpr 96
		.amdhsa_accum_offset 208
		.amdhsa_reserve_vcc 1
		.amdhsa_float_round_mode_32 0
		.amdhsa_float_round_mode_16_64 0
		.amdhsa_float_denorm_mode_32 3
		.amdhsa_float_denorm_mode_16_64 3
		.amdhsa_dx10_clamp 1
		.amdhsa_ieee_mode 1
		.amdhsa_fp16_overflow 0
		.amdhsa_tg_split 0
		.amdhsa_exception_fp_ieee_invalid_op 0
		.amdhsa_exception_fp_denorm_src 0
		.amdhsa_exception_fp_ieee_div_zero 0
		.amdhsa_exception_fp_ieee_overflow 0
		.amdhsa_exception_fp_ieee_underflow 0
		.amdhsa_exception_fp_ieee_inexact 0
		.amdhsa_exception_int_div_zero 0
	.end_amdhsa_kernel

amdhsa.kernels:
  - .agpr_count:     0
    .args:
      - .actual_access:  read_only
        .address_space:  global
        .offset:         0
        .size:           8
        .value_kind:     global_buffer
      - .actual_access:  read_only
        .address_space:  global
        .offset:         8
        .size:           8
        .value_kind:     global_buffer
      - .actual_access:  read_only
        .address_space:  global
        .offset:         16
        .size:           8
        .value_kind:     global_buffer
      - .actual_access:  read_only
        .address_space:  global
        .offset:         24
        .size:           8
        .value_kind:     global_buffer
      - .actual_access:  read_only
        .address_space:  global
        .offset:         32
        .size:           8
        .value_kind:     global_buffer
      - .actual_access:  write_only
        .address_space:  global
        .offset:         40
        .size:           8
        .value_kind:     global_buffer
      - .actual_access:  write_only
        .address_space:  global
        .offset:         48
        .size:           8
        .value_kind:     global_buffer
      - .actual_access:  write_only
        .address_space:  global
        .offset:         56
        .size:           8
        .value_kind:     global_buffer
    .group_segment_fixed_size: 0
    .kernarg_segment_align: 8
    .kernarg_segment_size: 64
    .language:       OpenCL C
    .language_version:
      - 2
      - 0
    .max_flat_workgroup_size: 256
    .name:           _Z11prep_kernelPKfS0_S0_S0_S0_PDv8_DF16_S2_Pi
    .private_segment_fixed_size: 0
    .sgpr_count:     26
    .sgpr_spill_count: 0
    .symbol:         _Z11prep_kernelPKfS0_S0_S0_S0_PDv8_DF16_S2_Pi.kd
    .uniform_work_group_size: 1
    .uses_dynamic_stack: false
    .vgpr_count:     18
    .vgpr_spill_count: 0
    .wavefront_size: 64
  - .agpr_count:     0
    .args:
      - .actual_access:  read_only
        .address_space:  global
        .offset:         0
        .size:           8
        .value_kind:     global_buffer
      - .actual_access:  read_only
        .address_space:  global
        .offset:         8
        .size:           8
        .value_kind:     global_buffer
      - .actual_access:  read_only
        .address_space:  global
        .offset:         16
        .size:           8
        .value_kind:     global_buffer
      - .actual_access:  read_only
        .address_space:  global
        .offset:         24
        .size:           8
        .value_kind:     global_buffer
      - .actual_access:  read_only
        .address_space:  global
        .offset:         32
        .size:           8
        .value_kind:     global_buffer
      - .actual_access:  read_only
        .address_space:  global
        .offset:         40
        .size:           8
        .value_kind:     global_buffer
      - .actual_access:  read_only
        .address_space:  global
        .offset:         48
        .size:           8
        .value_kind:     global_buffer
      - .actual_access:  read_only
        .address_space:  global
        .offset:         56
        .size:           8
        .value_kind:     global_buffer
      - .actual_access:  read_only
        .address_space:  global
        .offset:         64
        .size:           8
        .value_kind:     global_buffer
      - .actual_access:  read_only
        .address_space:  global
        .offset:         72
        .size:           8
        .value_kind:     global_buffer
      - .actual_access:  read_only
        .address_space:  global
        .offset:         80
        .size:           8
        .value_kind:     global_buffer
      - .actual_access:  read_only
        .address_space:  global
        .offset:         88
        .size:           8
        .value_kind:     global_buffer
      - .actual_access:  read_only
        .address_space:  global
        .offset:         96
        .size:           8
        .value_kind:     global_buffer
      - .actual_access:  read_only
        .address_space:  global
        .offset:         104
        .size:           8
        .value_kind:     global_buffer
      - .actual_access:  write_only
        .address_space:  global
        .offset:         112
        .size:           8
        .value_kind:     global_buffer
      - .offset:         120
        .size:           4
        .value_kind:     by_value
      - .actual_access:  read_only
        .address_space:  global
        .offset:         128
        .size:           8
        .value_kind:     global_buffer
      - .actual_access:  read_only
        .address_space:  global
        .offset:         136
        .size:           8
        .value_kind:     global_buffer
      - .actual_access:  write_only
        .address_space:  global
        .offset:         144
        .size:           8
        .value_kind:     global_buffer
      - .actual_access:  read_only
        .address_space:  global
        .offset:         152
        .size:           8
        .value_kind:     global_buffer
      - .actual_access:  read_only
        .address_space:  global
        .offset:         160
        .size:           8
        .value_kind:     global_buffer
      - .address_space:  global
        .offset:         168
        .size:           8
        .value_kind:     global_buffer
      - .actual_access:  write_only
        .address_space:  global
        .offset:         176
        .size:           8
        .value_kind:     global_buffer
      - .address_space:  global
        .offset:         184
        .size:           8
        .value_kind:     global_buffer
      - .actual_access:  write_only
        .address_space:  global
        .offset:         192
        .size:           8
        .value_kind:     global_buffer
      - .actual_access:  write_only
        .address_space:  global
        .offset:         200
        .size:           8
        .value_kind:     global_buffer
    .group_segment_fixed_size: 21760
    .kernarg_segment_align: 8
    .kernarg_segment_size: 208
    .language:       OpenCL C
    .language_version:
      - 2
      - 0
    .max_flat_workgroup_size: 256
    .name:           _Z12embed_kernelPKiS0_S0_S0_S0_PKfS2_S2_S2_S2_S2_S2_S2_PKDv8_DF16_PfiS2_S2_PS3_S0_S0_PiS8_S8_P15HIP_vector_typeIiLj2EES8_
    .private_segment_fixed_size: 0
    .sgpr_count:     44
    .sgpr_spill_count: 0
    .symbol:         _Z12embed_kernelPKiS0_S0_S0_S0_PKfS2_S2_S2_S2_S2_S2_S2_PKDv8_DF16_PfiS2_S2_PS3_S0_S0_PiS8_S8_P15HIP_vector_typeIiLj2EES8_.kd
    .uniform_work_group_size: 1
    .uses_dynamic_stack: false
    .vgpr_count:     166
    .vgpr_spill_count: 0
    .wavefront_size: 64
  - .agpr_count:     0
    .args:
      - .actual_access:  read_only
        .address_space:  global
        .offset:         0
        .size:           8
        .value_kind:     global_buffer
      - .actual_access:  read_only
        .address_space:  global
        .offset:         8
        .size:           8
        .value_kind:     global_buffer
      - .actual_access:  read_only
        .address_space:  global
        .offset:         16
        .size:           8
        .value_kind:     global_buffer
      - .actual_access:  read_only
        .address_space:  global
        .offset:         24
        .size:           8
        .value_kind:     global_buffer
      - .actual_access:  read_only
        .address_space:  global
        .offset:         32
        .size:           8
        .value_kind:     global_buffer
      - .actual_access:  read_only
        .address_space:  global
        .offset:         40
        .size:           8
        .value_kind:     global_buffer
      - .actual_access:  read_only
        .address_space:  global
        .offset:         48
        .size:           8
        .value_kind:     global_buffer
      - .actual_access:  read_only
        .address_space:  global
        .offset:         56
        .size:           8
        .value_kind:     global_buffer
      - .actual_access:  write_only
        .address_space:  global
        .offset:         64
        .size:           8
        .value_kind:     global_buffer
      - .offset:         72
        .size:           4
        .value_kind:     by_value
    .group_segment_fixed_size: 30720
    .kernarg_segment_align: 8
    .kernarg_segment_size: 76
    .language:       OpenCL C
    .language_version:
      - 2
      - 0
    .max_flat_workgroup_size: 256
    .name:           _Z10gru_kernelPKfPKiS2_S2_PK15HIP_vector_typeIiLj2EEPKDv8_DF16_S0_S0_Pfi
    .private_segment_fixed_size: 0
    .sgpr_count:     31
    .sgpr_spill_count: 0
    .symbol:         _Z10gru_kernelPKfPKiS2_S2_PK15HIP_vector_typeIiLj2EEPKDv8_DF16_S0_S0_Pfi.kd
    .uniform_work_group_size: 1
    .uses_dynamic_stack: false
    .vgpr_count:     230
    .vgpr_spill_count: 0
    .wavefront_size: 64
  - .agpr_count:     0
    .args:
      - .actual_access:  read_only
        .address_space:  global
        .offset:         0
        .size:           8
        .value_kind:     global_buffer
      - .actual_access:  read_only
        .address_space:  global
        .offset:         8
        .size:           8
        .value_kind:     global_buffer
      - .actual_access:  write_only
        .address_space:  global
        .offset:         16
        .size:           8
        .value_kind:     global_buffer
    .group_segment_fixed_size: 1024
    .kernarg_segment_align: 8
    .kernarg_segment_size: 24
    .language:       OpenCL C
    .language_version:
      - 2
      - 0
    .max_flat_workgroup_size: 256
    .name:           _Z11pool_kernelPKfPKiPDF16_
    .private_segment_fixed_size: 0
    .sgpr_count:     16
    .sgpr_spill_count: 0
    .symbol:         _Z11pool_kernelPKfPKiPDF16_.kd
    .uniform_work_group_size: 1
    .uses_dynamic_stack: false
    .vgpr_count:     18
    .vgpr_spill_count: 0
    .wavefront_size: 64
  - .agpr_count:     0
    .args:
      - .actual_access:  read_only
        .address_space:  global
        .offset:         0
        .size:           8
        .value_kind:     global_buffer
      - .actual_access:  read_only
        .address_space:  global
        .offset:         8
        .size:           8
        .value_kind:     global_buffer
      - .actual_access:  write_only
        .address_space:  global
        .offset:         16
        .size:           8
        .value_kind:     global_buffer
    .group_segment_fixed_size: 73728
    .kernarg_segment_align: 8
    .kernarg_segment_size: 24
    .language:       OpenCL C
    .language_version:
      - 2
      - 0
    .max_flat_workgroup_size: 256
    .name:           _Z9fc_kernelPKDv8_DF16_S1_Pf
    .private_segment_fixed_size: 0
    .sgpr_count:     17
    .sgpr_spill_count: 0
    .symbol:         _Z9fc_kernelPKDv8_DF16_S1_Pf.kd
    .uniform_work_group_size: 1
    .uses_dynamic_stack: false
    .vgpr_count:     208
    .vgpr_spill_count: 0
    .wavefront_size: 64
